# attention: fragment ds_reads issued first after the per-tile barrier; the five K/V LDS-DMA groups issued one each behind the first five QK^T MFMAs
# speedup vs baseline: 1.0140x; 1.0140x over previous
.LBB0_757:
	s_add_i32 s6, 0, 0x12000
	v_add_u32_e32 v199, s6, v170
	v_add_u32_e32 v204, s6, v171
	v_add_u32_e32 v205, s6, v172
	ds_read_b128 v[64:67], v180 offset:49152
	ds_read_b128 v[68:71], v180 offset:57344
	ds_read_b128 v[200:203], v181 offset:49152
	ds_read_b128 v[226:229], v181 offset:57344
	ds_read_b128 v[230:233], v182 offset:49152
	ds_read_b128 v[234:237], v182 offset:57344
	ds_read_b128 v[238:241], v183 offset:49152
	ds_read_b128 v[242:245], v183 offset:57344
	s_waitcnt lgkmcnt(7)
	v_mfma_f32_32x32x16_bf16 v[80:95], v[64:67], v[124:127], 0
	s_add_i32 s12, s64, -1
	s_sub_i32 s80, s11, 64
	s_cmp_lt_u32 s12, 3
	s_cselect_b32 s80, s10, s80
	s_mul_i32 s81, s80, 0xc00
	s_add_i32 s85, s82, 0x8000
	s_mov_b32 m0, s85
	s_add_i32 s85, s82, 0x10000
	buffer_load_dwordx4 v154, s[72:75], s81 offen lds
	v_exp_f32_e32 v216, v128
	v_add_f32_e32 v128, 0, v222
	v_add_f32_e32 v128, v224, v128
	v_add_f32_e32 v128, v220, v128
	v_add_f32_e32 v128, v223, v128
	v_add_f32_e32 v128, v219, v128
	v_add_f32_e32 v128, v221, v128
	s_waitcnt lgkmcnt(6)
	v_mfma_f32_32x32x16_bf16 v[64:79], v[68:71], v[124:127], 0
	s_mov_b32 m0, s85
	s_add_i32 s85, s82, 0xa000
	buffer_load_dwordx4 v155, s[72:75], s81 offen lds
	v_add_f32_e32 v128, v217, v128
	v_add_f32_e32 v128, v218, v128
	v_add_f32_e32 v128, v212, v128
	v_add_f32_e32 v128, v214, v128
	v_add_f32_e32 v128, v211, v128
	v_add_f32_e32 v128, v213, v128
	v_exp_f32_e32 v138, v138
	s_waitcnt lgkmcnt(5)
	v_mfma_f32_32x32x16_bf16 v[80:95], v[200:203], v[120:123], v[80:95]
	s_mov_b32 m0, s85
	s_add_i32 s81, s81, 0x18000
	buffer_load_dwordx4 v154, s[72:75], s81 offen lds
	v_add_f32_e32 v128, v208, v128
	v_exp_f32_e32 v139, v139
	v_add_f32_e32 v128, v210, v128
	v_exp_f32_e32 v164, v136
	v_add_f32_e32 v128, v207, v128
	v_exp_f32_e32 v137, v137
	v_add_f32_e32 v128, v209, v128
	s_waitcnt lgkmcnt(4)
	v_mfma_f32_32x32x16_bf16 v[64:79], v[226:229], v[120:123], v[64:79]
	s_lshl_b32 s81, s83, 11
	s_add_i32 s85, s82, 0x4000
	s_mov_b32 m0, s85
	s_add_i32 s85, s82, 0x6000
	buffer_load_dwordx4 v158, s[76:79], s81 offen lds
	ds_read_b128 v[200:203], v184 offset:49152
	ds_read_b128 v[226:229], v184 offset:57344
	v_exp_f32_e32 v165, v132
	v_add_f32_e32 v128, v138, v128
	v_add_f32_e32 v128, v139, v128
	v_exp_f32_e32 v206, v130
	v_add_f32_e32 v128, v164, v128
	v_exp_f32_e32 v215, v131
	s_waitcnt lgkmcnt(5)
	v_mfma_f32_32x32x16_bf16 v[80:95], v[230:233], v[116:119], v[80:95]
	s_mov_b32 m0, s85
	s_add_i32 s81, s81, 0x10000
	buffer_load_dwordx4 v158, s[76:79], s81 offen lds
	s_mov_b32 s84, s80
	v_add_f32_e32 v128, v137, v128
	v_add_f32_e32 v128, v165, v128
	v_exp_f32_e32 v225, v129
	v_exp_f32_e32 v162, v162
	v_exp_f32_e32 v163, v163
	v_exp_f32_e32 v160, v160
	v_exp_f32_e32 v161, v161
	s_waitcnt lgkmcnt(4)
	v_mfma_f32_32x32x16_bf16 v[64:79], v[234:237], v[116:119], v[64:79]
	ds_read_b128 v[230:233], v185 offset:49152
	ds_read_b128 v[234:237], v185 offset:57344
	v_cvt_pk_bf16_f32 v129, v220, v223
	v_cvt_pk_bf16_f32 v130, v219, v221
	v_cvt_pk_bf16_f32 v131, v217, v218
	v_cvt_pk_bf16_f32 v132, v212, v214
	v_cvt_pk_bf16_f32 v136, v138, v139
	v_cvt_pk_bf16_f32 v137, v164, v137
	s_waitcnt lgkmcnt(5)
	v_mfma_f32_32x32x16_bf16 v[80:95], v[238:241], v[112:115], v[80:95]
	v_cvt_pk_bf16_f32 v139, v206, v215
	v_permlane32_swap_b32_e32 v129, v131
	s_nop 0
	v_permlane32_swap_b32_e32 v137, v139
	s_waitcnt lgkmcnt(4)
	v_mfma_f32_32x32x16_bf16 v[64:79], v[242:245], v[112:115], v[64:79]
	ds_read_b128 v[238:241], v186 offset:49152
	ds_read_b128 v[242:245], v186 offset:57344
	s_waitcnt lgkmcnt(5)
	v_mfma_f32_32x32x16_bf16 v[80:95], v[200:203], v[108:111], v[80:95]
	s_waitcnt lgkmcnt(4)
	v_mfma_f32_32x32x16_bf16 v[64:79], v[226:229], v[108:111], v[64:79]
	ds_read_b128 v[200:203], v187 offset:49152
	ds_read_b128 v[226:229], v187 offset:57344
	s_waitcnt lgkmcnt(5)
	v_mfma_f32_32x32x16_bf16 v[80:95], v[230:233], v[104:107], v[80:95]
	s_waitcnt lgkmcnt(4)
	v_mfma_f32_32x32x16_bf16 v[64:79], v[234:237], v[104:107], v[64:79]
	ds_read_b128 v[230:233], v199
	ds_read_b128 v[234:237], v199 offset:4096
	ds_read_b128 v[246:249], v190
	s_waitcnt lgkmcnt(6)
	v_mfma_f32_32x32x16_bf16 v[80:95], v[238:241], v[100:103], v[80:95]
	s_waitcnt lgkmcnt(5)
	v_mfma_f32_32x32x16_bf16 v[64:79], v[242:245], v[100:103], v[64:79]
	ds_read_b128 v[238:241], v204
	ds_read_b128 v[242:245], v204 offset:4096
	ds_read_b128 v[250:253], v190 offset:1024
	v_add_u32_e32 v204, s6, v173
	s_waitcnt lgkmcnt(7)
	v_mfma_f32_32x32x16_bf16 v[80:95], v[200:203], v[96:99], v[80:95]
	s_waitcnt lgkmcnt(6)
	v_mfma_f32_32x32x16_bf16 v[64:79], v[226:229], v[96:99], v[64:79]
	ds_read_b128 v[200:203], v205
	ds_read_b128 v[226:229], v205 offset:4096
	s_waitcnt lgkmcnt(5)
	v_mfma_f32_32x32x16_bf16 v[80:95], v[230:233], v[246:249], v[80:95]
	s_waitcnt lgkmcnt(5)
	v_mfma_f32_32x32x16_bf16 v[64:79], v[234:237], v[246:249], v[64:79]
	ds_read_b128 v[230:233], v204
	ds_read_b128 v[234:237], v204 offset:4096
	ds_read_b128 v[246:249], v190 offset:2048
	s_waitcnt lgkmcnt(5)
	v_mfma_f32_32x32x16_bf16 v[80:95], v[238:241], v[250:253], v[80:95]
	s_waitcnt lgkmcnt(5)
	v_mfma_f32_32x32x16_bf16 v[64:79], v[242:245], v[250:253], v[64:79]
	ds_read_b128 v[250:253], v190 offset:3072
	s_waitcnt lgkmcnt(1)
	v_mfma_f32_32x32x16_bf16 v[80:95], v[200:203], v[246:249], v[80:95]
	v_exp_f32_e32 v205, v133
	v_cvt_pk_bf16_f32 v133, v211, v213
	v_cvt_pk_bf16_f32 v138, v165, v205
	v_add_f32_e32 v128, v205, v128
	v_add_f32_e32 v128, v206, v128
	v_add_f32_e32 v128, v215, v128
	s_waitcnt lgkmcnt(1)
	v_mfma_f32_32x32x16_bf16 v[64:79], v[226:229], v[246:249], v[64:79]
	v_add_f32_e32 v128, v216, v128
	v_add_f32_e32 v128, v225, v128
	v_add_f32_e32 v128, v162, v128
	v_add_f32_e32 v128, v163, v128
	v_add_f32_e32 v128, v160, v128
	v_add_f32_e32 v128, v161, v128
	s_waitcnt lgkmcnt(0)
	v_mfma_f32_32x32x16_bf16 v[80:95], v[230:233], v[250:253], v[80:95]
	v_exp_f32_e32 v226, v134
	v_exp_f32_e32 v227, v135
	v_cvt_pk_bf16_f32 v134, v208, v210
	v_cvt_pk_bf16_f32 v135, v207, v209
	v_add_f32_e32 v128, v226, v128
	v_add_f32_e32 v203, v227, v128
	v_mov_b32_e32 v204, v203
	s_waitcnt lgkmcnt(0)
	v_mfma_f32_32x32x16_bf16 v[64:79], v[234:237], v[250:253], v[64:79]
	s_nop 0
	v_permlane32_swap_b32_e32 v203, v204
	v_cvt_pk_bf16_f32 v128, v222, v224
	v_cvt_pk_bf16_f32 v208, v216, v225
	v_cvt_pk_bf16_f32 v209, v162, v163
	v_cvt_pk_bf16_f32 v210, v160, v161
	v_cvt_pk_bf16_f32 v211, v226, v227
	v_permlane32_swap_b32_e32 v132, v134
	v_permlane32_swap_b32_e32 v128, v130
	v_permlane32_swap_b32_e32 v133, v135
	v_permlane32_swap_b32_e32 v136, v138
	v_permlane32_swap_b32_e32 v208, v210
	v_permlane32_swap_b32_e32 v209, v211
	ds_read_b64_tr_b16 v[160:161], v167 offset:0
	ds_read_b64_tr_b16 v[162:163], v167 offset:0x800
	ds_read_b64_tr_b16 v[232:233], v167 offset:0x1000
	ds_read_b64_tr_b16 v[234:235], v167 offset:0x1800
	ds_read_b64_tr_b16 v[236:237], v167 offset:0x2000
	ds_read_b64_tr_b16 v[238:239], v167 offset:0x2800
	ds_read_b64_tr_b16 v[240:241], v167 offset:0x3000
	ds_read_b64_tr_b16 v[242:243], v167 offset:0x3800
	v_max_f32_e32 v164, v81, v81
	v_max_f32_e32 v165, v80, v80
	v_max_f32_e32 v164, v165, v164
	v_max3_f32 v164, v164, v82, v83
	v_max3_f32 v164, v164, v84, v85
	v_max3_f32 v164, v164, v86, v87
	v_max3_f32 v164, v164, v88, v89
	v_max3_f32 v164, v164, v90, v91
	v_max3_f32 v164, v164, v92, v93
	v_max3_f32 v164, v164, v94, v95
	s_waitcnt lgkmcnt(0)
	v_mfma_f32_32x32x16_bf16 v[16:31], v[128:131], v[160:163], v[16:31]
	v_max3_f32 v160, v164, v64, v65
	v_max3_f32 v160, v160, v66, v67
	v_max3_f32 v160, v160, v68, v69
	v_mfma_f32_32x32x16_bf16 v[16:31], v[132:135], v[232:235], v[16:31]
	ds_read_b64_tr_b16 v[232:233], v167 offset:0x200
	ds_read_b64_tr_b16 v[234:235], v167 offset:0xa00
	v_max3_f32 v160, v160, v70, v71
	v_max3_f32 v160, v160, v72, v73
	v_max3_f32 v160, v160, v74, v75
	v_mfma_f32_32x32x16_bf16 v[16:31], v[136:139], v[236:239], v[16:31]
	ds_read_b64_tr_b16 v[236:237], v167 offset:0x1200
	ds_read_b64_tr_b16 v[238:239], v167 offset:0x1a00
	ds_read_b64_tr_b16 v[244:245], v167 offset:0x2200
	ds_read_b64_tr_b16 v[246:247], v167 offset:0x2a00
	ds_read_b64_tr_b16 v[248:249], v167 offset:0x3200
	ds_read_b64_tr_b16 v[250:251], v167 offset:0x3a00
	v_max3_f32 v160, v160, v76, v77
	v_max3_f32 v160, v160, v78, v79
	v_mov_b32_e32 v161, v160
	v_mfma_f32_32x32x16_bf16 v[16:31], v[208:211], v[240:243], v[16:31]
	v_max_f32_e32 v162, v198, v198
	v_permlane32_swap_b32_e32 v160, v161
	v_max_f32_e32 v161, v161, v161
	v_max_f32_e32 v160, v160, v160
	v_max_f32_e32 v160, v160, v161
	s_waitcnt lgkmcnt(0)
	v_mfma_f32_32x32x16_bf16 v[32:47], v[128:131], v[232:235], v[32:47]
	ds_read_b64_tr_b16 v[232:233], v167 offset:0x400
	ds_read_b64_tr_b16 v[234:235], v167 offset:0xc00
	v_sub_f32_e32 v161, v160, v198
	v_max_f32_e32 v160, v162, v160
	v_sub_f32_e32 v162, v198, v160
	v_mul_f32_e32 v162, 0x3dd53b94, v162
	v_exp_f32_e32 v162, v162
	v_mfma_f32_32x32x16_bf16 v[32:47], v[132:135], v[236:239], v[32:47]
	ds_read_b64_tr_b16 v[236:237], v167 offset:0x1400
	ds_read_b64_tr_b16 v[238:239], v167 offset:0x1c00
	ds_read_b64_tr_b16 v[240:241], v167 offset:0x2400
	ds_read_b64_tr_b16 v[242:243], v167 offset:0x2c00
	v_cmp_ge_f32_e32 vcc, s48, v161
	s_cmp_eq_u64 vcc, exec
	s_cselect_b64 s[6:7], -1, 0
	v_cndmask_b32_e64 v206, v162, 1.0, s[6:7]
	v_cndmask_b32_e64 v160, v160, v198, s[6:7]
	v_mul_f32_e32 v205, 0xbdd53b94, v160
	v_cmp_gt_f32_e32 vcc, 1.0, v206
	v_mfma_f32_32x32x16_bf16 v[32:47], v[136:139], v[244:247], v[32:47]
	ds_read_b64_tr_b16 v[244:245], v167 offset:0x3400
	ds_read_b64_tr_b16 v[246:247], v167 offset:0x3c00
	v_fmamk_f32 v87, v87, 0x3dd53b94, v205
	v_fmamk_f32 v80, v80, 0x3dd53b94, v205
	v_fmamk_f32 v81, v81, 0x3dd53b94, v205
	v_fmamk_f32 v82, v82, 0x3dd53b94, v205
	v_fmamk_f32 v83, v83, 0x3dd53b94, v205
	v_mfma_f32_32x32x16_bf16 v[32:47], v[208:211], v[248:251], v[32:47]
	v_fmamk_f32 v84, v84, 0x3dd53b94, v205
	v_fmamk_f32 v85, v85, 0x3dd53b94, v205
	v_fmamk_f32 v86, v86, 0x3dd53b94, v205
	v_fmamk_f32 v88, v88, 0x3dd53b94, v205
	v_fmamk_f32 v89, v89, 0x3dd53b94, v205
	s_waitcnt lgkmcnt(0)
	v_mfma_f32_32x32x16_bf16 v[0:15], v[128:131], v[232:235], v[0:15]
	ds_read_b64_tr_b16 v[232:233], v167 offset:0x600
	ds_read_b64_tr_b16 v[234:235], v167 offset:0xe00
	v_fmamk_f32 v90, v90, 0x3dd53b94, v205
	v_fmamk_f32 v91, v91, 0x3dd53b94, v205
	v_fmamk_f32 v92, v92, 0x3dd53b94, v205
	v_fmamk_f32 v93, v93, 0x3dd53b94, v205
	v_fmamk_f32 v94, v94, 0x3dd53b94, v205
	v_mfma_f32_32x32x16_bf16 v[0:15], v[132:135], v[236:239], v[0:15]
	ds_read_b64_tr_b16 v[236:237], v167 offset:0x1600
	ds_read_b64_tr_b16 v[238:239], v167 offset:0x1e00
	v_fmamk_f32 v95, v95, 0x3dd53b94, v205
	v_fmamk_f32 v215, v64, 0x3dd53b94, v205
	v_fmamk_f32 v216, v65, 0x3dd53b94, v205
	v_fmamk_f32 v217, v66, 0x3dd53b94, v205
	v_fmamk_f32 v218, v67, 0x3dd53b94, v205
	v_mfma_f32_32x32x16_bf16 v[0:15], v[136:139], v[240:243], v[0:15]
	ds_read_b64_tr_b16 v[240:241], v167 offset:0x2600
	ds_read_b64_tr_b16 v[242:243], v167 offset:0x2e00
	ds_read_b64_tr_b16 v[248:249], v167 offset:0x3600
	ds_read_b64_tr_b16 v[250:251], v167 offset:0x3e00
	v_fmamk_f32 v219, v68, 0x3dd53b94, v205
	v_fmamk_f32 v212, v73, 0x3dd53b94, v205
	v_fmamk_f32 v213, v74, 0x3dd53b94, v205
	v_fmamk_f32 v214, v75, 0x3dd53b94, v205
	v_mfma_f32_32x32x16_bf16 v[0:15], v[208:211], v[244:247], v[0:15]
	v_fmamk_f32 v207, v76, 0x3dd53b94, v205
	v_fmamk_f32 v220, v77, 0x3dd53b94, v205
	v_fmamk_f32 v221, v78, 0x3dd53b94, v205
	s_waitcnt lgkmcnt(0)
	v_mfma_f32_32x32x16_bf16 v[48:63], v[128:131], v[232:235], v[48:63]
	v_exp_f32_e32 v128, v80
	v_exp_f32_e32 v129, v82
	v_exp_f32_e32 v130, v84
	v_exp_f32_e32 v131, v86
	v_mfma_f32_32x32x16_bf16 v[48:63], v[132:135], v[236:239], v[48:63]
	v_exp_f32_e32 v132, v88
	v_exp_f32_e32 v133, v90
	v_exp_f32_e32 v134, v92
	v_exp_f32_e32 v135, v94
	v_mfma_f32_32x32x16_bf16 v[48:63], v[136:139], v[240:243], v[48:63]
	v_exp_f32_e32 v139, v89
	v_exp_f32_e32 v138, v91
	v_exp_f32_e32 v137, v93
	v_exp_f32_e32 v136, v95
	v_mfma_f32_32x32x16_bf16 v[48:63], v[208:211], v[248:251], v[48:63]
	v_exp_f32_e32 v161, v87
	v_exp_f32_e32 v198, v81
	v_exp_f32_e32 v163, v83
	v_exp_f32_e32 v162, v85
	v_fmamk_f32 v208, v69, 0x3dd53b94, v205
	v_fmamk_f32 v209, v70, 0x3dd53b94, v205
	v_fmamk_f32 v210, v71, 0x3dd53b94, v205
	v_fmamk_f32 v211, v72, 0x3dd53b94, v205
	v_fmac_f32_e32 v205, 0x3dd53b94, v79
	s_cbranch_vccz .LBB0_761
	s_and_saveexec_b64 s[8:9], s[4:5]
	ds_write_b32 v189, v206 offset:128
	s_or_b64 exec, exec, s[8:9]
	s_waitcnt lgkmcnt(0)
	v_add_u32_e32 v248, s62, v169
	ds_read_b128 v[232:235], v248 offset:224
	ds_read_b128 v[236:239], v248 offset:192
	ds_read_b128 v[240:243], v248 offset:160
	ds_read_b128 v[244:247], v248 offset:128
	s_waitcnt lgkmcnt(3)
	v_pk_mul_f32 v[28:29], v[28:29], v[232:233]
	s_waitcnt lgkmcnt(2)
	v_pk_mul_f32 v[24:25], v[24:25], v[236:237]
	s_waitcnt lgkmcnt(1)
	v_pk_mul_f32 v[20:21], v[20:21], v[240:241]
	v_pk_mul_f32 v[30:31], v[30:31], v[234:235]
	v_pk_mul_f32 v[26:27], v[26:27], v[238:239]
	v_pk_mul_f32 v[22:23], v[22:23], v[242:243]
	s_waitcnt lgkmcnt(0)
	v_pk_mul_f32 v[18:19], v[18:19], v[246:247]
	v_pk_mul_f32 v[16:17], v[16:17], v[244:245]
	v_pk_mul_f32 v[44:45], v[44:45], v[232:233]
	v_pk_mul_f32 v[40:41], v[40:41], v[236:237]
	v_pk_mul_f32 v[36:37], v[36:37], v[240:241]
	v_pk_mul_f32 v[46:47], v[46:47], v[234:235]
	v_pk_mul_f32 v[42:43], v[42:43], v[238:239]
	v_pk_mul_f32 v[38:39], v[38:39], v[242:243]
	v_pk_mul_f32 v[34:35], v[34:35], v[246:247]
	v_pk_mul_f32 v[32:33], v[32:33], v[244:245]
	v_pk_mul_f32 v[12:13], v[12:13], v[232:233]
	v_pk_mul_f32 v[8:9], v[8:9], v[236:237]
	v_pk_mul_f32 v[4:5], v[4:5], v[240:241]
	v_pk_mul_f32 v[14:15], v[14:15], v[234:235]
	v_pk_mul_f32 v[10:11], v[10:11], v[238:239]
	v_pk_mul_f32 v[6:7], v[6:7], v[242:243]
	v_pk_mul_f32 v[2:3], v[2:3], v[246:247]
	v_pk_mul_f32 v[0:1], v[0:1], v[244:245]
	v_pk_mul_f32 v[60:61], v[60:61], v[232:233]
	v_pk_mul_f32 v[56:57], v[56:57], v[236:237]
	v_pk_mul_f32 v[52:53], v[52:53], v[240:241]
	v_pk_mul_f32 v[62:63], v[62:63], v[234:235]
	v_pk_mul_f32 v[58:59], v[58:59], v[238:239]
	v_pk_mul_f32 v[54:55], v[54:55], v[242:243]
	v_pk_mul_f32 v[50:51], v[50:51], v[246:247]
	v_pk_mul_f32 v[48:49], v[48:49], v[244:245]
.LBB0_761:
	s_waitcnt vmcnt(0) lgkmcnt(0)
	s_barrier
	ds_read_b128 v[64:67], v180 offset:32768
	ds_read_b128 v[68:71], v180 offset:40960
	ds_read_b128 v[222:225], v181 offset:32768
	ds_read_b128 v[226:229], v181 offset:40960
	ds_read_b128 v[230:233], v182 offset:32768
	ds_read_b128 v[234:237], v182 offset:40960
	ds_read_b128 v[238:241], v183 offset:32768
	ds_read_b128 v[242:245], v183 offset:40960
	v_exp_f32_e32 v164, v215
	v_add_f32_e32 v215, 0, v128
	s_waitcnt lgkmcnt(7)
	v_mfma_f32_32x32x16_bf16 v[80:95], v[64:67], v[124:127], 0
	s_add_i32 s80, s10, 64
	s_cmp_lt_u32 s12, 2
	s_cselect_b32 s80, s80, s11
	s_mul_i32 s81, s80, 0xc00
	s_add_i32 s85, s82, 0xc000
	s_mov_b32 m0, s85
	s_add_i32 s85, s82, 0x12000
	buffer_load_dwordx4 v154, s[72:75], s81 offen lds
	v_add_f32_e32 v215, v198, v215
	v_add_f32_e32 v215, v129, v215
	v_add_f32_e32 v215, v163, v215
	v_add_f32_e32 v215, v130, v215
	v_add_f32_e32 v215, v162, v215
	v_add_f32_e32 v215, v131, v215
	v_add_f32_e32 v215, v161, v215
	s_waitcnt lgkmcnt(6)
	v_mfma_f32_32x32x16_bf16 v[64:79], v[68:71], v[124:127], 0
	s_mov_b32 m0, s85
	s_add_i32 s85, s82, 0xe000
	buffer_load_dwordx4 v155, s[72:75], s81 offen lds
	v_add_f32_e32 v215, v132, v215
	v_add_f32_e32 v215, v139, v215
	v_add_f32_e32 v215, v133, v215
	v_add_f32_e32 v215, v138, v215
	v_add_f32_e32 v215, v134, v215
	v_exp_f32_e32 v165, v216
	v_add_f32_e32 v215, v137, v215
	s_waitcnt lgkmcnt(5)
	v_mfma_f32_32x32x16_bf16 v[80:95], v[222:225], v[120:123], v[80:95]
	s_mov_b32 m0, s85
	s_add_i32 s81, s81, 0x18000
	buffer_load_dwordx4 v154, s[72:75], s81 offen lds
	v_exp_f32_e32 v217, v217
	v_add_f32_e32 v215, v135, v215
	v_exp_f32_e32 v218, v218
	v_add_f32_e32 v215, v136, v215
	v_exp_f32_e32 v219, v219
	v_add_f32_e32 v215, v164, v215
	v_exp_f32_e32 v208, v208
	s_waitcnt lgkmcnt(4)
	v_mfma_f32_32x32x16_bf16 v[64:79], v[226:229], v[120:123], v[64:79]
	s_lshl_b32 s81, s84, 11
	s_add_i32 s85, s82, 0x0
	s_mov_b32 m0, s85
	s_add_i32 s85, s82, 0x2000
	buffer_load_dwordx4 v158, s[76:79], s81 offen lds
	ds_read_b128 v[222:225], v184 offset:32768
	ds_read_b128 v[226:229], v184 offset:40960
	v_add_f32_e32 v215, v165, v215
	v_exp_f32_e32 v209, v209
	v_add_f32_e32 v215, v217, v215
	v_exp_f32_e32 v210, v210
	v_add_f32_e32 v215, v218, v215
	v_exp_f32_e32 v211, v211
	s_waitcnt lgkmcnt(5)
	v_mfma_f32_32x32x16_bf16 v[80:95], v[230:233], v[116:119], v[80:95]
	s_mov_b32 m0, s85
	s_add_i32 s81, s81, 0x10000
	buffer_load_dwordx4 v158, s[76:79], s81 offen lds
	s_mov_b32 s83, s80
	v_add_f32_e32 v215, v219, v215
	v_exp_f32_e32 v212, v212
	v_add_f32_e32 v215, v208, v215
	v_exp_f32_e32 v213, v213
	v_add_f32_e32 v215, v209, v215
	v_exp_f32_e32 v214, v214
	v_add_f32_e32 v215, v210, v215
	s_waitcnt lgkmcnt(4)
	v_mfma_f32_32x32x16_bf16 v[64:79], v[234:237], v[116:119], v[64:79]
	ds_read_b128 v[230:233], v185 offset:32768
	ds_read_b128 v[234:237], v185 offset:40960
	v_exp_f32_e32 v207, v207
	v_add_f32_e32 v215, v211, v215
	v_exp_f32_e32 v220, v220
	v_add_f32_e32 v215, v212, v215
	v_exp_f32_e32 v221, v221
	v_add_f32_e32 v215, v213, v215
	s_waitcnt lgkmcnt(5)
	v_mfma_f32_32x32x16_bf16 v[80:95], v[238:241], v[112:115], v[80:95]
	v_exp_f32_e32 v205, v205
	v_add_f32_e32 v215, v214, v215
	v_add_f32_e32 v215, v207, v215
	v_add_f32_e32 v215, v220, v215
	v_add_f32_e32 v215, v221, v215
	v_add_f32_e32 v215, v205, v215
	v_mov_b32_e32 v216, v215
	s_waitcnt lgkmcnt(4)
	v_mfma_f32_32x32x16_bf16 v[64:79], v[242:245], v[112:115], v[64:79]
	ds_read_b128 v[238:241], v186 offset:32768
	ds_read_b128 v[242:245], v186 offset:40960
	v_permlane32_swap_b32_e32 v215, v216
	v_cvt_pk_bf16_f32 v128, v128, v198
	v_cvt_pk_bf16_f32 v129, v129, v163
	v_cvt_pk_bf16_f32 v130, v130, v162
	v_cvt_pk_bf16_f32 v131, v131, v161
	s_waitcnt lgkmcnt(5)
	v_mfma_f32_32x32x16_bf16 v[80:95], v[222:225], v[108:111], v[80:95]
	v_cvt_pk_bf16_f32 v132, v132, v139
	v_cvt_pk_bf16_f32 v133, v133, v138
	v_cvt_pk_bf16_f32 v134, v134, v137
	v_cvt_pk_bf16_f32 v135, v135, v136
	v_cvt_pk_bf16_f32 v136, v164, v165
	v_cvt_pk_bf16_f32 v137, v217, v218
	v_cvt_pk_bf16_f32 v138, v219, v208
	s_waitcnt lgkmcnt(4)
	v_mfma_f32_32x32x16_bf16 v[64:79], v[226:229], v[108:111], v[64:79]
	ds_read_b128 v[222:225], v187 offset:32768
	ds_read_b128 v[226:229], v187 offset:40960
	v_cvt_pk_bf16_f32 v139, v209, v210
	v_cvt_pk_bf16_f32 v208, v211, v212
	v_cvt_pk_bf16_f32 v209, v213, v214
	v_cvt_pk_bf16_f32 v210, v207, v220
	v_cvt_pk_bf16_f32 v211, v221, v205
	v_permlane32_swap_b32_e32 v128, v130
	s_waitcnt lgkmcnt(5)
	v_mfma_f32_32x32x16_bf16 v[80:95], v[230:233], v[104:107], v[80:95]
	v_permlane32_swap_b32_e32 v129, v131
	v_permlane32_swap_b32_e32 v132, v134
	v_permlane32_swap_b32_e32 v133, v135
	v_permlane32_swap_b32_e32 v136, v138
	s_waitcnt lgkmcnt(4)
	v_mfma_f32_32x32x16_bf16 v[64:79], v[234:237], v[104:107], v[64:79]
	ds_read_b128 v[230:233], v191
	ds_read_b128 v[234:237], v191 offset:4096
	ds_read_b128 v[246:249], v190
	v_permlane32_swap_b32_e32 v137, v139
	v_permlane32_swap_b32_e32 v208, v210
	v_permlane32_swap_b32_e32 v209, v211
	s_waitcnt lgkmcnt(6)
	v_mfma_f32_32x32x16_bf16 v[80:95], v[238:241], v[100:103], v[80:95]
	s_waitcnt lgkmcnt(5)
	v_mfma_f32_32x32x16_bf16 v[64:79], v[242:245], v[100:103], v[64:79]
	ds_read_b128 v[238:241], v192
	ds_read_b128 v[242:245], v192 offset:4096
	ds_read_b128 v[250:253], v190 offset:1024
	s_waitcnt lgkmcnt(7)
	v_mfma_f32_32x32x16_bf16 v[80:95], v[222:225], v[96:99], v[80:95]
	s_waitcnt lgkmcnt(6)
	v_mfma_f32_32x32x16_bf16 v[64:79], v[226:229], v[96:99], v[64:79]
	ds_read_b128 v[222:225], v193
	ds_read_b128 v[226:229], v193 offset:4096
	s_waitcnt lgkmcnt(5)
	v_mfma_f32_32x32x16_bf16 v[80:95], v[230:233], v[246:249], v[80:95]
	s_waitcnt lgkmcnt(5)
	v_mfma_f32_32x32x16_bf16 v[64:79], v[234:237], v[246:249], v[64:79]
	ds_read_b128 v[230:233], v194
	ds_read_b128 v[234:237], v194 offset:4096
	ds_read_b128 v[246:249], v190 offset:2048
	s_waitcnt lgkmcnt(5)
	v_mfma_f32_32x32x16_bf16 v[80:95], v[238:241], v[250:253], v[80:95]
	s_waitcnt lgkmcnt(5)
	v_mfma_f32_32x32x16_bf16 v[64:79], v[242:245], v[250:253], v[64:79]
	ds_read_b128 v[250:253], v190 offset:3072
	s_waitcnt lgkmcnt(1)
	v_mfma_f32_32x32x16_bf16 v[80:95], v[222:225], v[246:249], v[80:95]
	s_waitcnt lgkmcnt(1)
	v_mfma_f32_32x32x16_bf16 v[64:79], v[226:229], v[246:249], v[64:79]
	s_waitcnt lgkmcnt(0)
	v_mfma_f32_32x32x16_bf16 v[80:95], v[230:233], v[250:253], v[80:95]
	s_waitcnt lgkmcnt(0)
	v_mfma_f32_32x32x16_bf16 v[64:79], v[234:237], v[250:253], v[64:79]
	ds_read_b64_tr_b16 v[238:239], v174 offset:0
	ds_read_b64_tr_b16 v[240:241], v174 offset:0x800
	ds_read_b64_tr_b16 v[242:243], v174 offset:0x1000
	ds_read_b64_tr_b16 v[244:245], v174 offset:0x1800
	ds_read_b64_tr_b16 v[246:247], v174 offset:0x2000
	ds_read_b64_tr_b16 v[248:249], v174 offset:0x2800
	ds_read_b64_tr_b16 v[250:251], v174 offset:0x3000
	ds_read_b64_tr_b16 v[252:253], v174 offset:0x3800
	s_nop 3
	v_max_f32_e32 v161, v81, v81
	v_max_f32_e32 v162, v80, v80
	v_max_f32_e32 v161, v162, v161
	v_max3_f32 v161, v161, v82, v83
	v_max3_f32 v161, v161, v84, v85
	v_max3_f32 v161, v161, v86, v87
	v_max3_f32 v161, v161, v88, v89
	v_max3_f32 v161, v161, v90, v91
	v_max3_f32 v161, v161, v92, v93
	v_max3_f32 v161, v161, v94, v95
	s_waitcnt lgkmcnt(0)
	v_mfma_f32_32x32x16_bf16 v[16:31], v[128:131], v[238:241], v[16:31]
	ds_read_b64_tr_b16 v[238:239], v174 offset:0x200
	ds_read_b64_tr_b16 v[240:241], v174 offset:0xa00
	v_max3_f32 v161, v161, v64, v65
	v_max3_f32 v161, v161, v66, v67
	v_max3_f32 v161, v161, v68, v69
	v_mfma_f32_32x32x16_bf16 v[16:31], v[132:135], v[242:245], v[16:31]
	ds_read_b64_tr_b16 v[242:243], v174 offset:0x1200
	ds_read_b64_tr_b16 v[244:245], v174 offset:0x1a00
	v_max3_f32 v161, v161, v70, v71
	v_max3_f32 v161, v161, v72, v73
	v_max3_f32 v161, v161, v74, v75
	v_mfma_f32_32x32x16_bf16 v[16:31], v[136:139], v[246:249], v[16:31]
	ds_read_b64_tr_b16 v[246:247], v174 offset:0x2200
	ds_read_b64_tr_b16 v[248:249], v174 offset:0x2a00
	ds_read_b64_tr_b16 v[162:163], v174 offset:0x3200
	ds_read_b64_tr_b16 v[164:165], v174 offset:0x3a00
	v_max3_f32 v161, v161, v76, v77
	v_max3_f32 v161, v161, v78, v79
	v_mov_b32_e32 v198, v161
	v_mfma_f32_32x32x16_bf16 v[16:31], v[208:211], v[250:253], v[16:31]
	v_max_f32_e32 v205, v160, v160
	v_permlane32_swap_b32_e32 v161, v198
	v_max_f32_e32 v198, v198, v198
	v_max_f32_e32 v161, v161, v161
	v_max_f32_e32 v161, v161, v198
	s_waitcnt lgkmcnt(0)
	v_mfma_f32_32x32x16_bf16 v[32:47], v[128:131], v[238:241], v[32:47]
	ds_read_b64_tr_b16 v[238:239], v174 offset:0x400
	ds_read_b64_tr_b16 v[240:241], v174 offset:0xc00
	v_sub_f32_e32 v198, v161, v160
	v_max_f32_e32 v161, v205, v161
	v_sub_f32_e32 v205, v160, v161
	v_mul_f32_e32 v205, 0x3dd53b94, v205
	v_exp_f32_e32 v205, v205
	v_mfma_f32_32x32x16_bf16 v[32:47], v[132:135], v[242:245], v[32:47]
	ds_read_b64_tr_b16 v[242:243], v174 offset:0x1400
	ds_read_b64_tr_b16 v[244:245], v174 offset:0x1c00
	v_cmp_ge_f32_e32 vcc, s48, v198
	s_cmp_eq_u64 vcc, exec
	s_cselect_b64 s[6:7], -1, 0
	v_cndmask_b32_e64 v205, v205, 1.0, s[6:7]
	v_cndmask_b32_e64 v198, v161, v160, s[6:7]
	v_mul_f32_e32 v236, 0xbdd53b94, v198
	v_mov_b32_e32 v237, v236
	v_cmp_gt_f32_e32 vcc, 1.0, v205
	v_mfma_f32_32x32x16_bf16 v[32:47], v[136:139], v[246:249], v[32:47]
	ds_read_b64_tr_b16 v[246:247], v174 offset:0x2400
	ds_read_b64_tr_b16 v[248:249], v174 offset:0x2c00
	ds_read_b64_tr_b16 v[250:251], v174 offset:0x3400
	ds_read_b64_tr_b16 v[252:253], v174 offset:0x3c00
	v_fmamk_f32 v80, v80, 0x3dd53b94, v236
	v_fmamk_f32 v81, v81, 0x3dd53b94, v236
	v_fmamk_f32 v82, v82, 0x3dd53b94, v236
	v_fmamk_f32 v83, v83, 0x3dd53b94, v236
	v_mfma_f32_32x32x16_bf16 v[32:47], v[208:211], v[162:165], v[32:47]
	v_fmamk_f32 v84, v84, 0x3dd53b94, v236
	v_fmamk_f32 v85, v85, 0x3dd53b94, v236
	v_fmamk_f32 v86, v86, 0x3dd53b94, v236
	v_fmamk_f32 v87, v87, 0x3dd53b94, v236
	s_waitcnt lgkmcnt(0)
	v_mfma_f32_32x32x16_bf16 v[0:15], v[128:131], v[238:241], v[0:15]
	ds_read_b64_tr_b16 v[162:163], v174 offset:0x600
	ds_read_b64_tr_b16 v[164:165], v174 offset:0xe00
	ds_read_b64_tr_b16 v[238:239], v174 offset:0x1600
	ds_read_b64_tr_b16 v[240:241], v174 offset:0x1e00
	v_fmamk_f32 v88, v88, 0x3dd53b94, v236
	v_fmamk_f32 v89, v89, 0x3dd53b94, v236
	v_fmamk_f32 v90, v90, 0x3dd53b94, v236
	v_fmamk_f32 v91, v91, 0x3dd53b94, v236
	v_mfma_f32_32x32x16_bf16 v[0:15], v[132:135], v[242:245], v[0:15]
	ds_read_b64_tr_b16 v[242:243], v174 offset:0x2600
	ds_read_b64_tr_b16 v[244:245], v174 offset:0x2e00
	v_fmamk_f32 v92, v92, 0x3dd53b94, v236
	v_fmamk_f32 v93, v93, 0x3dd53b94, v236
	v_fmamk_f32 v94, v94, 0x3dd53b94, v236
	v_fmamk_f32 v95, v95, 0x3dd53b94, v236
	v_mfma_f32_32x32x16_bf16 v[0:15], v[136:139], v[246:249], v[0:15]
	ds_read_b64_tr_b16 v[246:247], v174 offset:0x3600
	ds_read_b64_tr_b16 v[248:249], v174 offset:0x3e00
	v_exp_f32_e32 v222, v80
	v_exp_f32_e32 v224, v81
	v_exp_f32_e32 v220, v82
	v_mfma_f32_32x32x16_bf16 v[0:15], v[208:211], v[250:253], v[0:15]
	v_exp_f32_e32 v223, v83
	v_exp_f32_e32 v219, v84
	v_exp_f32_e32 v221, v85
	s_waitcnt lgkmcnt(0)
	v_mfma_f32_32x32x16_bf16 v[48:63], v[128:131], v[162:165], v[48:63]
	v_exp_f32_e32 v217, v86
	v_exp_f32_e32 v218, v87
	v_exp_f32_e32 v212, v88
	v_pk_fma_f32 v[130:131], v[70:71], s[28:29], v[236:237] op_sel_hi:[1,0,0]
	v_pk_fma_f32 v[128:129], v[72:73], s[28:29], v[236:237] op_sel_hi:[1,0,0]
	v_mfma_f32_32x32x16_bf16 v[48:63], v[132:135], v[238:241], v[48:63]
	v_exp_f32_e32 v214, v89
	v_exp_f32_e32 v213, v91
	v_exp_f32_e32 v207, v94
	v_pk_fma_f32 v[132:133], v[68:69], s[28:29], v[236:237] op_sel_hi:[1,0,0]
	v_pk_fma_f32 v[134:135], v[78:79], s[28:29], v[236:237] op_sel_hi:[1,0,0]
	v_mfma_f32_32x32x16_bf16 v[48:63], v[136:139], v[242:245], v[48:63]
	v_pk_fma_f32 v[138:139], v[64:65], s[28:29], v[236:237] op_sel_hi:[1,0,0]
	v_pk_fma_f32 v[136:137], v[66:67], s[28:29], v[236:237] op_sel_hi:[1,0,0]
	v_pk_fma_f32 v[162:163], v[74:75], s[28:29], v[236:237] op_sel_hi:[1,0,0]
	v_pk_fma_f32 v[160:161], v[76:77], s[28:29], v[236:237] op_sel_hi:[1,0,0]
	v_mfma_f32_32x32x16_bf16 v[48:63], v[208:211], v[246:249], v[48:63]
	v_exp_f32_e32 v211, v90
	v_exp_f32_e32 v208, v92
	v_exp_f32_e32 v210, v93
	v_exp_f32_e32 v209, v95
	v_add_f32_e32 v64, v203, v204
	v_fmac_f32_e32 v64, v197, v140
	v_add_f32_e32 v140, v215, v216
	s_addk_i32 s10, 0x80
	s_add_i32 s64, s64, 2
	s_addk_i32 s11, 0x80
	v_fmac_f32_e32 v140, v64, v206
	s_cbranch_vccz .LBB0_765
	s_and_saveexec_b64 s[8:9], s[4:5]
	ds_write_b32 v189, v205 offset:128
	s_or_b64 exec, exec, s[8:9]
	s_waitcnt lgkmcnt(0)
	v_add_u32_e32 v164, s62, v169
	ds_read_b128 v[238:241], v164 offset:224
	ds_read_b128 v[242:245], v164 offset:192
	ds_read_b128 v[246:249], v164 offset:160
	ds_read_b128 v[250:253], v164 offset:128
	s_waitcnt lgkmcnt(3)
	v_pk_mul_f32 v[28:29], v[28:29], v[238:239]
	s_waitcnt lgkmcnt(2)
	v_pk_mul_f32 v[24:25], v[24:25], v[242:243]
	s_waitcnt lgkmcnt(1)
	v_pk_mul_f32 v[20:21], v[20:21], v[246:247]
	v_pk_mul_f32 v[30:31], v[30:31], v[240:241]
	v_pk_mul_f32 v[26:27], v[26:27], v[244:245]
	v_pk_mul_f32 v[22:23], v[22:23], v[248:249]
	s_waitcnt lgkmcnt(0)
	v_pk_mul_f32 v[18:19], v[18:19], v[252:253]
	v_pk_mul_f32 v[16:17], v[16:17], v[250:251]
	v_pk_mul_f32 v[44:45], v[44:45], v[238:239]
	v_pk_mul_f32 v[40:41], v[40:41], v[242:243]
	v_pk_mul_f32 v[36:37], v[36:37], v[246:247]
	v_pk_mul_f32 v[46:47], v[46:47], v[240:241]
	v_pk_mul_f32 v[42:43], v[42:43], v[244:245]
	v_pk_mul_f32 v[38:39], v[38:39], v[248:249]
	v_pk_mul_f32 v[34:35], v[34:35], v[252:253]
	v_pk_mul_f32 v[32:33], v[32:33], v[250:251]
	v_pk_mul_f32 v[12:13], v[12:13], v[238:239]
	v_pk_mul_f32 v[8:9], v[8:9], v[242:243]
	v_pk_mul_f32 v[4:5], v[4:5], v[246:247]
	v_pk_mul_f32 v[14:15], v[14:15], v[240:241]
	v_pk_mul_f32 v[10:11], v[10:11], v[244:245]
	v_pk_mul_f32 v[6:7], v[6:7], v[248:249]
	v_pk_mul_f32 v[2:3], v[2:3], v[252:253]
	v_pk_mul_f32 v[0:1], v[0:1], v[250:251]
	v_pk_mul_f32 v[60:61], v[60:61], v[238:239]
	v_pk_mul_f32 v[56:57], v[56:57], v[242:243]
	v_pk_mul_f32 v[52:53], v[52:53], v[246:247]
	v_pk_mul_f32 v[62:63], v[62:63], v[240:241]
	v_pk_mul_f32 v[58:59], v[58:59], v[244:245]
	v_pk_mul_f32 v[54:55], v[54:55], v[248:249]
	v_pk_mul_f32 v[50:51], v[50:51], v[252:253]
	v_pk_mul_f32 v[48:49], v[48:49], v[250:251]

.LBB0_2012:
	s_add_i32 s6, 0, 0x12000
	v_add_u32_e32 v199, s6, v170
	v_add_u32_e32 v204, s6, v171
	v_add_u32_e32 v205, s6, v172
	ds_read_b128 v[64:67], v180 offset:49152
	ds_read_b128 v[68:71], v180 offset:57344
	ds_read_b128 v[200:203], v181 offset:49152
	ds_read_b128 v[226:229], v181 offset:57344
	ds_read_b128 v[230:233], v182 offset:49152
	ds_read_b128 v[234:237], v182 offset:57344
	ds_read_b128 v[238:241], v183 offset:49152
	ds_read_b128 v[242:245], v183 offset:57344
	s_waitcnt lgkmcnt(7)
	v_mfma_f32_32x32x16_bf16 v[80:95], v[64:67], v[124:127], 0
	s_add_i32 s8, s8, 2
	s_sub_i32 s80, s14, 64
	s_cmp_lt_u32 s8, 3
	s_cselect_b32 s80, s13, s80
	s_mul_i32 s81, s80, 0xc00
	s_add_i32 s85, s82, 0x8000
	s_mov_b32 m0, s85
	s_add_i32 s85, s82, 0x10000
	buffer_load_dwordx4 v154, s[72:75], s81 offen lds
	v_exp_f32_e32 v216, v128
	v_add_f32_e32 v128, 0, v222
	v_add_f32_e32 v128, v224, v128
	v_add_f32_e32 v128, v220, v128
	v_add_f32_e32 v128, v223, v128
	v_add_f32_e32 v128, v219, v128
	v_add_f32_e32 v128, v221, v128
	s_waitcnt lgkmcnt(6)
	v_mfma_f32_32x32x16_bf16 v[64:79], v[68:71], v[124:127], 0
	s_mov_b32 m0, s85
	s_add_i32 s85, s82, 0xa000
	buffer_load_dwordx4 v155, s[72:75], s81 offen lds
	v_add_f32_e32 v128, v217, v128
	v_add_f32_e32 v128, v218, v128
	v_add_f32_e32 v128, v212, v128
	v_add_f32_e32 v128, v214, v128
	v_add_f32_e32 v128, v211, v128
	v_add_f32_e32 v128, v213, v128
	v_exp_f32_e32 v138, v138
	s_waitcnt lgkmcnt(5)
	v_mfma_f32_32x32x16_bf16 v[80:95], v[200:203], v[120:123], v[80:95]
	s_mov_b32 m0, s85
	s_add_i32 s81, s81, 0x18000
	buffer_load_dwordx4 v154, s[72:75], s81 offen lds
	v_add_f32_e32 v128, v208, v128
	v_exp_f32_e32 v139, v139
	v_add_f32_e32 v128, v210, v128
	v_exp_f32_e32 v164, v136
	v_add_f32_e32 v128, v207, v128
	v_exp_f32_e32 v137, v137
	v_add_f32_e32 v128, v209, v128
	s_waitcnt lgkmcnt(4)
	v_mfma_f32_32x32x16_bf16 v[64:79], v[226:229], v[120:123], v[64:79]
	s_lshl_b32 s81, s83, 11
	s_add_i32 s85, s82, 0x4000
	s_mov_b32 m0, s85
	s_add_i32 s85, s82, 0x6000
	buffer_load_dwordx4 v158, s[76:79], s81 offen lds
	ds_read_b128 v[200:203], v184 offset:49152
	ds_read_b128 v[226:229], v184 offset:57344
	v_exp_f32_e32 v165, v132
	v_add_f32_e32 v128, v138, v128
	v_add_f32_e32 v128, v139, v128
	v_exp_f32_e32 v206, v130
	v_add_f32_e32 v128, v164, v128
	v_exp_f32_e32 v215, v131
	s_waitcnt lgkmcnt(5)
	v_mfma_f32_32x32x16_bf16 v[80:95], v[230:233], v[116:119], v[80:95]
	s_mov_b32 m0, s85
	s_add_i32 s81, s81, 0x10000
	buffer_load_dwordx4 v158, s[76:79], s81 offen lds
	s_mov_b32 s84, s80
	v_add_f32_e32 v128, v137, v128
	v_add_f32_e32 v128, v165, v128
	v_exp_f32_e32 v225, v129
	v_exp_f32_e32 v162, v162
	v_exp_f32_e32 v163, v163
	v_exp_f32_e32 v160, v160
	v_exp_f32_e32 v161, v161
	s_waitcnt lgkmcnt(4)
	v_mfma_f32_32x32x16_bf16 v[64:79], v[234:237], v[116:119], v[64:79]
	ds_read_b128 v[230:233], v185 offset:49152
	ds_read_b128 v[234:237], v185 offset:57344
	v_cvt_pk_bf16_f32 v129, v220, v223
	v_cvt_pk_bf16_f32 v130, v219, v221
	v_cvt_pk_bf16_f32 v131, v217, v218
	v_cvt_pk_bf16_f32 v132, v212, v214
	v_cvt_pk_bf16_f32 v136, v138, v139
	v_cvt_pk_bf16_f32 v137, v164, v137
	s_waitcnt lgkmcnt(5)
	v_mfma_f32_32x32x16_bf16 v[80:95], v[238:241], v[112:115], v[80:95]
	v_cvt_pk_bf16_f32 v139, v206, v215
	v_permlane32_swap_b32_e32 v129, v131
	s_nop 0
	v_permlane32_swap_b32_e32 v137, v139
	s_waitcnt lgkmcnt(4)
	v_mfma_f32_32x32x16_bf16 v[64:79], v[242:245], v[112:115], v[64:79]
	ds_read_b128 v[238:241], v186 offset:49152
	ds_read_b128 v[242:245], v186 offset:57344
	s_waitcnt lgkmcnt(5)
	v_mfma_f32_32x32x16_bf16 v[80:95], v[200:203], v[108:111], v[80:95]
	s_waitcnt lgkmcnt(4)
	v_mfma_f32_32x32x16_bf16 v[64:79], v[226:229], v[108:111], v[64:79]
	ds_read_b128 v[200:203], v187 offset:49152
	ds_read_b128 v[226:229], v187 offset:57344
	s_waitcnt lgkmcnt(5)
	v_mfma_f32_32x32x16_bf16 v[80:95], v[230:233], v[104:107], v[80:95]
	s_waitcnt lgkmcnt(4)
	v_mfma_f32_32x32x16_bf16 v[64:79], v[234:237], v[104:107], v[64:79]
	ds_read_b128 v[230:233], v199
	ds_read_b128 v[234:237], v199 offset:4096
	ds_read_b128 v[246:249], v190
	s_waitcnt lgkmcnt(6)
	v_mfma_f32_32x32x16_bf16 v[80:95], v[238:241], v[100:103], v[80:95]
	s_waitcnt lgkmcnt(5)
	v_mfma_f32_32x32x16_bf16 v[64:79], v[242:245], v[100:103], v[64:79]
	ds_read_b128 v[238:241], v204
	ds_read_b128 v[242:245], v204 offset:4096
	ds_read_b128 v[250:253], v190 offset:1024
	v_add_u32_e32 v204, s6, v173
	s_waitcnt lgkmcnt(7)
	v_mfma_f32_32x32x16_bf16 v[80:95], v[200:203], v[96:99], v[80:95]
	s_waitcnt lgkmcnt(6)
	v_mfma_f32_32x32x16_bf16 v[64:79], v[226:229], v[96:99], v[64:79]
	ds_read_b128 v[200:203], v205
	ds_read_b128 v[226:229], v205 offset:4096
	s_waitcnt lgkmcnt(5)
	v_mfma_f32_32x32x16_bf16 v[80:95], v[230:233], v[246:249], v[80:95]
	s_waitcnt lgkmcnt(5)
	v_mfma_f32_32x32x16_bf16 v[64:79], v[234:237], v[246:249], v[64:79]
	ds_read_b128 v[230:233], v204
	ds_read_b128 v[234:237], v204 offset:4096
	ds_read_b128 v[246:249], v190 offset:2048
	s_waitcnt lgkmcnt(5)
	v_mfma_f32_32x32x16_bf16 v[80:95], v[238:241], v[250:253], v[80:95]
	s_waitcnt lgkmcnt(5)
	v_mfma_f32_32x32x16_bf16 v[64:79], v[242:245], v[250:253], v[64:79]
	ds_read_b128 v[250:253], v190 offset:3072
	s_waitcnt lgkmcnt(1)
	v_mfma_f32_32x32x16_bf16 v[80:95], v[200:203], v[246:249], v[80:95]
	v_exp_f32_e32 v205, v133
	v_cvt_pk_bf16_f32 v133, v211, v213
	v_cvt_pk_bf16_f32 v138, v165, v205
	v_add_f32_e32 v128, v205, v128
	v_add_f32_e32 v128, v206, v128
	v_add_f32_e32 v128, v215, v128
	s_waitcnt lgkmcnt(1)
	v_mfma_f32_32x32x16_bf16 v[64:79], v[226:229], v[246:249], v[64:79]
	v_add_f32_e32 v128, v216, v128
	v_add_f32_e32 v128, v225, v128
	v_add_f32_e32 v128, v162, v128
	v_add_f32_e32 v128, v163, v128
	v_add_f32_e32 v128, v160, v128
	v_add_f32_e32 v128, v161, v128
	s_waitcnt lgkmcnt(0)
	v_mfma_f32_32x32x16_bf16 v[80:95], v[230:233], v[250:253], v[80:95]
	v_exp_f32_e32 v226, v134
	v_exp_f32_e32 v227, v135
	v_cvt_pk_bf16_f32 v134, v208, v210
	v_cvt_pk_bf16_f32 v135, v207, v209
	v_add_f32_e32 v128, v226, v128
	v_add_f32_e32 v203, v227, v128
	v_mov_b32_e32 v204, v203
	s_waitcnt lgkmcnt(0)
	v_mfma_f32_32x32x16_bf16 v[64:79], v[234:237], v[250:253], v[64:79]
	s_nop 0
	v_permlane32_swap_b32_e32 v203, v204
	v_cvt_pk_bf16_f32 v128, v222, v224
	v_cvt_pk_bf16_f32 v208, v216, v225
	v_cvt_pk_bf16_f32 v209, v162, v163
	v_cvt_pk_bf16_f32 v210, v160, v161
	v_cvt_pk_bf16_f32 v211, v226, v227
	v_permlane32_swap_b32_e32 v132, v134
	v_permlane32_swap_b32_e32 v128, v130
	v_permlane32_swap_b32_e32 v133, v135
	v_permlane32_swap_b32_e32 v136, v138
	v_permlane32_swap_b32_e32 v208, v210
	v_permlane32_swap_b32_e32 v209, v211
	ds_read_b64_tr_b16 v[160:161], v167 offset:0
	ds_read_b64_tr_b16 v[162:163], v167 offset:0x800
	ds_read_b64_tr_b16 v[232:233], v167 offset:0x1000
	ds_read_b64_tr_b16 v[234:235], v167 offset:0x1800
	ds_read_b64_tr_b16 v[236:237], v167 offset:0x2000
	ds_read_b64_tr_b16 v[238:239], v167 offset:0x2800
	ds_read_b64_tr_b16 v[240:241], v167 offset:0x3000
	ds_read_b64_tr_b16 v[242:243], v167 offset:0x3800
	v_max_f32_e32 v164, v81, v81
	v_max_f32_e32 v165, v80, v80
	v_max_f32_e32 v164, v165, v164
	v_max3_f32 v164, v164, v82, v83
	v_max3_f32 v164, v164, v84, v85
	v_max3_f32 v164, v164, v86, v87
	v_max3_f32 v164, v164, v88, v89
	v_max3_f32 v164, v164, v90, v91
	v_max3_f32 v164, v164, v92, v93
	v_max3_f32 v164, v164, v94, v95
	s_waitcnt lgkmcnt(0)
	v_mfma_f32_32x32x16_bf16 v[0:15], v[128:131], v[160:163], v[0:15]
	v_max3_f32 v160, v164, v64, v65
	v_max3_f32 v160, v160, v66, v67
	v_max3_f32 v160, v160, v68, v69
	v_mfma_f32_32x32x16_bf16 v[0:15], v[132:135], v[232:235], v[0:15]
	ds_read_b64_tr_b16 v[232:233], v167 offset:0x200
	ds_read_b64_tr_b16 v[234:235], v167 offset:0xa00
	v_max3_f32 v160, v160, v70, v71
	v_max3_f32 v160, v160, v72, v73
	v_max3_f32 v160, v160, v74, v75
	v_mfma_f32_32x32x16_bf16 v[0:15], v[136:139], v[236:239], v[0:15]
	ds_read_b64_tr_b16 v[236:237], v167 offset:0x1200
	ds_read_b64_tr_b16 v[238:239], v167 offset:0x1a00
	ds_read_b64_tr_b16 v[244:245], v167 offset:0x2200
	ds_read_b64_tr_b16 v[246:247], v167 offset:0x2a00
	ds_read_b64_tr_b16 v[248:249], v167 offset:0x3200
	ds_read_b64_tr_b16 v[250:251], v167 offset:0x3a00
	v_max3_f32 v160, v160, v76, v77
	v_max3_f32 v160, v160, v78, v79
	v_mov_b32_e32 v161, v160
	v_mfma_f32_32x32x16_bf16 v[0:15], v[208:211], v[240:243], v[0:15]
	v_max_f32_e32 v162, v198, v198
	v_permlane32_swap_b32_e32 v160, v161
	v_max_f32_e32 v161, v161, v161
	v_max_f32_e32 v160, v160, v160
	v_max_f32_e32 v160, v160, v161
	s_waitcnt lgkmcnt(0)
	v_mfma_f32_32x32x16_bf16 v[32:47], v[128:131], v[232:235], v[32:47]
	ds_read_b64_tr_b16 v[232:233], v167 offset:0x400
	ds_read_b64_tr_b16 v[234:235], v167 offset:0xc00
	v_sub_f32_e32 v161, v160, v198
	v_max_f32_e32 v160, v162, v160
	v_sub_f32_e32 v162, v198, v160
	v_mul_f32_e32 v162, 0x3dd53b94, v162
	v_exp_f32_e32 v162, v162
	v_mfma_f32_32x32x16_bf16 v[32:47], v[132:135], v[236:239], v[32:47]
	ds_read_b64_tr_b16 v[236:237], v167 offset:0x1400
	ds_read_b64_tr_b16 v[238:239], v167 offset:0x1c00
	ds_read_b64_tr_b16 v[240:241], v167 offset:0x2400
	ds_read_b64_tr_b16 v[242:243], v167 offset:0x2c00
	v_cmp_ge_f32_e32 vcc, s46, v161
	s_cmp_eq_u64 vcc, exec
	s_cselect_b64 s[6:7], -1, 0
	v_cndmask_b32_e64 v206, v162, 1.0, s[6:7]
	v_cndmask_b32_e64 v160, v160, v198, s[6:7]
	v_mul_f32_e32 v205, 0xbdd53b94, v160
	v_cmp_gt_f32_e32 vcc, 1.0, v206
	v_mfma_f32_32x32x16_bf16 v[32:47], v[136:139], v[244:247], v[32:47]
	ds_read_b64_tr_b16 v[244:245], v167 offset:0x3400
	ds_read_b64_tr_b16 v[246:247], v167 offset:0x3c00
	v_fmamk_f32 v87, v87, 0x3dd53b94, v205
	v_fmamk_f32 v80, v80, 0x3dd53b94, v205
	v_fmamk_f32 v81, v81, 0x3dd53b94, v205
	v_fmamk_f32 v82, v82, 0x3dd53b94, v205
	v_fmamk_f32 v83, v83, 0x3dd53b94, v205
	v_mfma_f32_32x32x16_bf16 v[32:47], v[208:211], v[248:251], v[32:47]
	v_fmamk_f32 v84, v84, 0x3dd53b94, v205
	v_fmamk_f32 v85, v85, 0x3dd53b94, v205
	v_fmamk_f32 v86, v86, 0x3dd53b94, v205
	v_fmamk_f32 v88, v88, 0x3dd53b94, v205
	v_fmamk_f32 v89, v89, 0x3dd53b94, v205
	s_waitcnt lgkmcnt(0)
	v_mfma_f32_32x32x16_bf16 v[16:31], v[128:131], v[232:235], v[16:31]
	ds_read_b64_tr_b16 v[232:233], v167 offset:0x600
	ds_read_b64_tr_b16 v[234:235], v167 offset:0xe00
	v_fmamk_f32 v90, v90, 0x3dd53b94, v205
	v_fmamk_f32 v91, v91, 0x3dd53b94, v205
	v_fmamk_f32 v92, v92, 0x3dd53b94, v205
	v_fmamk_f32 v93, v93, 0x3dd53b94, v205
	v_fmamk_f32 v94, v94, 0x3dd53b94, v205
	v_mfma_f32_32x32x16_bf16 v[16:31], v[132:135], v[236:239], v[16:31]
	ds_read_b64_tr_b16 v[236:237], v167 offset:0x1600
	ds_read_b64_tr_b16 v[238:239], v167 offset:0x1e00
	v_fmamk_f32 v95, v95, 0x3dd53b94, v205
	v_fmamk_f32 v215, v64, 0x3dd53b94, v205
	v_fmamk_f32 v216, v65, 0x3dd53b94, v205
	v_fmamk_f32 v217, v66, 0x3dd53b94, v205
	v_fmamk_f32 v218, v67, 0x3dd53b94, v205
	v_mfma_f32_32x32x16_bf16 v[16:31], v[136:139], v[240:243], v[16:31]
	ds_read_b64_tr_b16 v[240:241], v167 offset:0x2600
	ds_read_b64_tr_b16 v[242:243], v167 offset:0x2e00
	ds_read_b64_tr_b16 v[248:249], v167 offset:0x3600
	ds_read_b64_tr_b16 v[250:251], v167 offset:0x3e00
	v_fmamk_f32 v219, v68, 0x3dd53b94, v205
	v_fmamk_f32 v212, v73, 0x3dd53b94, v205
	v_fmamk_f32 v213, v74, 0x3dd53b94, v205
	v_fmamk_f32 v214, v75, 0x3dd53b94, v205
	v_mfma_f32_32x32x16_bf16 v[16:31], v[208:211], v[244:247], v[16:31]
	v_fmamk_f32 v207, v76, 0x3dd53b94, v205
	v_fmamk_f32 v220, v77, 0x3dd53b94, v205
	v_fmamk_f32 v221, v78, 0x3dd53b94, v205
	s_waitcnt lgkmcnt(0)
	v_mfma_f32_32x32x16_bf16 v[48:63], v[128:131], v[232:235], v[48:63]
	v_exp_f32_e32 v128, v80
	v_exp_f32_e32 v129, v82
	v_exp_f32_e32 v130, v84
	v_exp_f32_e32 v131, v86
	v_mfma_f32_32x32x16_bf16 v[48:63], v[132:135], v[236:239], v[48:63]
	v_exp_f32_e32 v132, v88
	v_exp_f32_e32 v133, v90
	v_exp_f32_e32 v134, v92
	v_exp_f32_e32 v135, v94
	v_mfma_f32_32x32x16_bf16 v[48:63], v[136:139], v[240:243], v[48:63]
	v_exp_f32_e32 v139, v89
	v_exp_f32_e32 v138, v91
	v_exp_f32_e32 v137, v93
	v_exp_f32_e32 v136, v95
	v_mfma_f32_32x32x16_bf16 v[48:63], v[208:211], v[248:251], v[48:63]
	v_exp_f32_e32 v161, v87
	v_exp_f32_e32 v198, v81
	v_exp_f32_e32 v163, v83
	v_exp_f32_e32 v162, v85
	v_fmamk_f32 v208, v69, 0x3dd53b94, v205
	v_fmamk_f32 v209, v70, 0x3dd53b94, v205
	v_fmamk_f32 v210, v71, 0x3dd53b94, v205
	v_fmamk_f32 v211, v72, 0x3dd53b94, v205
	v_fmac_f32_e32 v205, 0x3dd53b94, v79
	s_cbranch_vccz .LBB0_2016
	s_and_saveexec_b64 s[10:11], s[4:5]
	ds_write_b32 v189, v206 offset:128
	s_or_b64 exec, exec, s[10:11]
	s_waitcnt lgkmcnt(0)
	v_add_u32_e32 v248, s12, v169
	ds_read_b128 v[232:235], v248 offset:224
	ds_read_b128 v[236:239], v248 offset:192
	ds_read_b128 v[240:243], v248 offset:160
	ds_read_b128 v[244:247], v248 offset:128
	s_waitcnt lgkmcnt(3)
	v_pk_mul_f32 v[12:13], v[12:13], v[232:233]
	s_waitcnt lgkmcnt(2)
	v_pk_mul_f32 v[8:9], v[8:9], v[236:237]
	s_waitcnt lgkmcnt(1)
	v_pk_mul_f32 v[4:5], v[4:5], v[240:241]
	v_pk_mul_f32 v[14:15], v[14:15], v[234:235]
	v_pk_mul_f32 v[10:11], v[10:11], v[238:239]
	v_pk_mul_f32 v[6:7], v[6:7], v[242:243]
	s_waitcnt lgkmcnt(0)
	v_pk_mul_f32 v[2:3], v[2:3], v[246:247]
	v_pk_mul_f32 v[0:1], v[0:1], v[244:245]
	v_pk_mul_f32 v[44:45], v[44:45], v[232:233]
	v_pk_mul_f32 v[40:41], v[40:41], v[236:237]
	v_pk_mul_f32 v[36:37], v[36:37], v[240:241]
	v_pk_mul_f32 v[46:47], v[46:47], v[234:235]
	v_pk_mul_f32 v[42:43], v[42:43], v[238:239]
	v_pk_mul_f32 v[38:39], v[38:39], v[242:243]
	v_pk_mul_f32 v[34:35], v[34:35], v[246:247]
	v_pk_mul_f32 v[32:33], v[32:33], v[244:245]
	v_pk_mul_f32 v[28:29], v[28:29], v[232:233]
	v_pk_mul_f32 v[24:25], v[24:25], v[236:237]
	v_pk_mul_f32 v[20:21], v[20:21], v[240:241]
	v_pk_mul_f32 v[30:31], v[30:31], v[234:235]
	v_pk_mul_f32 v[26:27], v[26:27], v[238:239]
	v_pk_mul_f32 v[22:23], v[22:23], v[242:243]
	v_pk_mul_f32 v[18:19], v[18:19], v[246:247]
	v_pk_mul_f32 v[16:17], v[16:17], v[244:245]
	v_pk_mul_f32 v[60:61], v[60:61], v[232:233]
	v_pk_mul_f32 v[56:57], v[56:57], v[236:237]
	v_pk_mul_f32 v[52:53], v[52:53], v[240:241]
	v_pk_mul_f32 v[62:63], v[62:63], v[234:235]
	v_pk_mul_f32 v[58:59], v[58:59], v[238:239]
	v_pk_mul_f32 v[54:55], v[54:55], v[242:243]
	v_pk_mul_f32 v[50:51], v[50:51], v[246:247]
	v_pk_mul_f32 v[48:49], v[48:49], v[244:245]
.LBB0_2016:
	s_waitcnt vmcnt(0) lgkmcnt(0)
	s_barrier
	ds_read_b128 v[64:67], v180 offset:32768
	ds_read_b128 v[68:71], v180 offset:40960
	ds_read_b128 v[222:225], v181 offset:32768
	ds_read_b128 v[226:229], v181 offset:40960
	ds_read_b128 v[230:233], v182 offset:32768
	ds_read_b128 v[234:237], v182 offset:40960
	ds_read_b128 v[238:241], v183 offset:32768
	ds_read_b128 v[242:245], v183 offset:40960
	v_exp_f32_e32 v164, v215
	v_add_f32_e32 v215, 0, v128
	s_waitcnt lgkmcnt(7)
	v_mfma_f32_32x32x16_bf16 v[80:95], v[64:67], v[124:127], 0
	s_add_i32 s80, s13, 64
	s_cmp_lt_u32 s8, 2
	s_cselect_b32 s80, s80, s14
	s_mul_i32 s81, s80, 0xc00
	s_add_i32 s85, s82, 0xc000
	s_mov_b32 m0, s85
	s_add_i32 s85, s82, 0x12000
	buffer_load_dwordx4 v154, s[72:75], s81 offen lds
	v_add_f32_e32 v215, v198, v215
	v_add_f32_e32 v215, v129, v215
	v_add_f32_e32 v215, v163, v215
	v_add_f32_e32 v215, v130, v215
	v_add_f32_e32 v215, v162, v215
	v_add_f32_e32 v215, v131, v215
	v_add_f32_e32 v215, v161, v215
	s_waitcnt lgkmcnt(6)
	v_mfma_f32_32x32x16_bf16 v[64:79], v[68:71], v[124:127], 0
	s_mov_b32 m0, s85
	s_add_i32 s85, s82, 0xe000
	buffer_load_dwordx4 v155, s[72:75], s81 offen lds
	v_add_f32_e32 v215, v132, v215
	v_add_f32_e32 v215, v139, v215
	v_add_f32_e32 v215, v133, v215
	v_add_f32_e32 v215, v138, v215
	v_add_f32_e32 v215, v134, v215
	v_exp_f32_e32 v165, v216
	v_add_f32_e32 v215, v137, v215
	s_waitcnt lgkmcnt(5)
	v_mfma_f32_32x32x16_bf16 v[80:95], v[222:225], v[120:123], v[80:95]
	s_mov_b32 m0, s85
	s_add_i32 s81, s81, 0x18000
	buffer_load_dwordx4 v154, s[72:75], s81 offen lds
	v_exp_f32_e32 v217, v217
	v_add_f32_e32 v215, v135, v215
	v_exp_f32_e32 v218, v218
	v_add_f32_e32 v215, v136, v215
	v_exp_f32_e32 v219, v219
	v_add_f32_e32 v215, v164, v215
	v_exp_f32_e32 v208, v208
	s_waitcnt lgkmcnt(4)
	v_mfma_f32_32x32x16_bf16 v[64:79], v[226:229], v[120:123], v[64:79]
	s_lshl_b32 s81, s84, 11
	s_add_i32 s85, s82, 0x0
	s_mov_b32 m0, s85
	s_add_i32 s85, s82, 0x2000
	buffer_load_dwordx4 v158, s[76:79], s81 offen lds
	ds_read_b128 v[222:225], v184 offset:32768
	ds_read_b128 v[226:229], v184 offset:40960
	v_add_f32_e32 v215, v165, v215
	v_exp_f32_e32 v209, v209
	v_add_f32_e32 v215, v217, v215
	v_exp_f32_e32 v210, v210
	v_add_f32_e32 v215, v218, v215
	v_exp_f32_e32 v211, v211
	s_waitcnt lgkmcnt(5)
	v_mfma_f32_32x32x16_bf16 v[80:95], v[230:233], v[116:119], v[80:95]
	s_mov_b32 m0, s85
	s_add_i32 s81, s81, 0x10000
	buffer_load_dwordx4 v158, s[76:79], s81 offen lds
	s_mov_b32 s83, s80
	v_add_f32_e32 v215, v219, v215
	v_exp_f32_e32 v212, v212
	v_add_f32_e32 v215, v208, v215
	v_exp_f32_e32 v213, v213
	v_add_f32_e32 v215, v209, v215
	v_exp_f32_e32 v214, v214
	v_add_f32_e32 v215, v210, v215
	s_waitcnt lgkmcnt(4)
	v_mfma_f32_32x32x16_bf16 v[64:79], v[234:237], v[116:119], v[64:79]
	ds_read_b128 v[230:233], v185 offset:32768
	ds_read_b128 v[234:237], v185 offset:40960
	v_exp_f32_e32 v207, v207
	v_add_f32_e32 v215, v211, v215
	v_exp_f32_e32 v220, v220
	v_add_f32_e32 v215, v212, v215
	v_exp_f32_e32 v221, v221
	v_add_f32_e32 v215, v213, v215
	s_waitcnt lgkmcnt(5)
	v_mfma_f32_32x32x16_bf16 v[80:95], v[238:241], v[112:115], v[80:95]
	v_exp_f32_e32 v205, v205
	v_add_f32_e32 v215, v214, v215
	v_add_f32_e32 v215, v207, v215
	v_add_f32_e32 v215, v220, v215
	v_add_f32_e32 v215, v221, v215
	v_add_f32_e32 v215, v205, v215
	v_mov_b32_e32 v216, v215
	s_waitcnt lgkmcnt(4)
	v_mfma_f32_32x32x16_bf16 v[64:79], v[242:245], v[112:115], v[64:79]
	ds_read_b128 v[238:241], v186 offset:32768
	ds_read_b128 v[242:245], v186 offset:40960
	v_permlane32_swap_b32_e32 v215, v216
	v_cvt_pk_bf16_f32 v128, v128, v198
	v_cvt_pk_bf16_f32 v129, v129, v163
	v_cvt_pk_bf16_f32 v130, v130, v162
	v_cvt_pk_bf16_f32 v131, v131, v161
	s_waitcnt lgkmcnt(5)
	v_mfma_f32_32x32x16_bf16 v[80:95], v[222:225], v[108:111], v[80:95]
	v_cvt_pk_bf16_f32 v132, v132, v139
	v_cvt_pk_bf16_f32 v133, v133, v138
	v_cvt_pk_bf16_f32 v134, v134, v137
	v_cvt_pk_bf16_f32 v135, v135, v136
	v_cvt_pk_bf16_f32 v136, v164, v165
	v_cvt_pk_bf16_f32 v137, v217, v218
	v_cvt_pk_bf16_f32 v138, v219, v208
	s_waitcnt lgkmcnt(4)
	v_mfma_f32_32x32x16_bf16 v[64:79], v[226:229], v[108:111], v[64:79]
	ds_read_b128 v[222:225], v187 offset:32768
	ds_read_b128 v[226:229], v187 offset:40960
	v_cvt_pk_bf16_f32 v139, v209, v210
	v_cvt_pk_bf16_f32 v208, v211, v212
	v_cvt_pk_bf16_f32 v209, v213, v214
	v_cvt_pk_bf16_f32 v210, v207, v220
	v_cvt_pk_bf16_f32 v211, v221, v205
	v_permlane32_swap_b32_e32 v128, v130
	s_waitcnt lgkmcnt(5)
	v_mfma_f32_32x32x16_bf16 v[80:95], v[230:233], v[104:107], v[80:95]
	v_permlane32_swap_b32_e32 v129, v131
	v_permlane32_swap_b32_e32 v132, v134
	v_permlane32_swap_b32_e32 v133, v135
	v_permlane32_swap_b32_e32 v136, v138
	s_waitcnt lgkmcnt(4)
	v_mfma_f32_32x32x16_bf16 v[64:79], v[234:237], v[104:107], v[64:79]
	ds_read_b128 v[230:233], v191
	ds_read_b128 v[234:237], v191 offset:4096
	ds_read_b128 v[246:249], v190
	v_permlane32_swap_b32_e32 v137, v139
	v_permlane32_swap_b32_e32 v208, v210
	v_permlane32_swap_b32_e32 v209, v211
	s_waitcnt lgkmcnt(6)
	v_mfma_f32_32x32x16_bf16 v[80:95], v[238:241], v[100:103], v[80:95]
	s_waitcnt lgkmcnt(5)
	v_mfma_f32_32x32x16_bf16 v[64:79], v[242:245], v[100:103], v[64:79]
	ds_read_b128 v[238:241], v192
	ds_read_b128 v[242:245], v192 offset:4096
	ds_read_b128 v[250:253], v190 offset:1024
	s_waitcnt lgkmcnt(7)
	v_mfma_f32_32x32x16_bf16 v[80:95], v[222:225], v[96:99], v[80:95]
	s_waitcnt lgkmcnt(6)
	v_mfma_f32_32x32x16_bf16 v[64:79], v[226:229], v[96:99], v[64:79]
	ds_read_b128 v[222:225], v193
	ds_read_b128 v[226:229], v193 offset:4096
	s_waitcnt lgkmcnt(5)
	v_mfma_f32_32x32x16_bf16 v[80:95], v[230:233], v[246:249], v[80:95]
	s_waitcnt lgkmcnt(5)
	v_mfma_f32_32x32x16_bf16 v[64:79], v[234:237], v[246:249], v[64:79]
	ds_read_b128 v[230:233], v194
	ds_read_b128 v[234:237], v194 offset:4096
	ds_read_b128 v[246:249], v190 offset:2048
	s_waitcnt lgkmcnt(5)
	v_mfma_f32_32x32x16_bf16 v[80:95], v[238:241], v[250:253], v[80:95]
	s_waitcnt lgkmcnt(5)
	v_mfma_f32_32x32x16_bf16 v[64:79], v[242:245], v[250:253], v[64:79]
	ds_read_b128 v[250:253], v190 offset:3072
	s_waitcnt lgkmcnt(1)
	v_mfma_f32_32x32x16_bf16 v[80:95], v[222:225], v[246:249], v[80:95]
	s_waitcnt lgkmcnt(1)
	v_mfma_f32_32x32x16_bf16 v[64:79], v[226:229], v[246:249], v[64:79]
	s_waitcnt lgkmcnt(0)
	v_mfma_f32_32x32x16_bf16 v[80:95], v[230:233], v[250:253], v[80:95]
	s_waitcnt lgkmcnt(0)
	v_mfma_f32_32x32x16_bf16 v[64:79], v[234:237], v[250:253], v[64:79]
	ds_read_b64_tr_b16 v[238:239], v174 offset:0
	ds_read_b64_tr_b16 v[240:241], v174 offset:0x800
	ds_read_b64_tr_b16 v[242:243], v174 offset:0x1000
	ds_read_b64_tr_b16 v[244:245], v174 offset:0x1800
	ds_read_b64_tr_b16 v[246:247], v174 offset:0x2000
	ds_read_b64_tr_b16 v[248:249], v174 offset:0x2800
	ds_read_b64_tr_b16 v[250:251], v174 offset:0x3000
	ds_read_b64_tr_b16 v[252:253], v174 offset:0x3800
	s_nop 3
	v_max_f32_e32 v161, v81, v81
	v_max_f32_e32 v162, v80, v80
	v_max_f32_e32 v161, v162, v161
	v_max3_f32 v161, v161, v82, v83
	v_max3_f32 v161, v161, v84, v85
	v_max3_f32 v161, v161, v86, v87
	v_max3_f32 v161, v161, v88, v89
	v_max3_f32 v161, v161, v90, v91
	v_max3_f32 v161, v161, v92, v93
	v_max3_f32 v161, v161, v94, v95
	s_waitcnt lgkmcnt(0)
	v_mfma_f32_32x32x16_bf16 v[0:15], v[128:131], v[238:241], v[0:15]
	ds_read_b64_tr_b16 v[238:239], v174 offset:0x200
	ds_read_b64_tr_b16 v[240:241], v174 offset:0xa00
	v_max3_f32 v161, v161, v64, v65
	v_max3_f32 v161, v161, v66, v67
	v_max3_f32 v161, v161, v68, v69
	v_mfma_f32_32x32x16_bf16 v[0:15], v[132:135], v[242:245], v[0:15]
	ds_read_b64_tr_b16 v[242:243], v174 offset:0x1200
	ds_read_b64_tr_b16 v[244:245], v174 offset:0x1a00
	v_max3_f32 v161, v161, v70, v71
	v_max3_f32 v161, v161, v72, v73
	v_max3_f32 v161, v161, v74, v75
	v_mfma_f32_32x32x16_bf16 v[0:15], v[136:139], v[246:249], v[0:15]
	ds_read_b64_tr_b16 v[246:247], v174 offset:0x2200
	ds_read_b64_tr_b16 v[248:249], v174 offset:0x2a00
	ds_read_b64_tr_b16 v[162:163], v174 offset:0x3200
	ds_read_b64_tr_b16 v[164:165], v174 offset:0x3a00
	v_max3_f32 v161, v161, v76, v77
	v_max3_f32 v161, v161, v78, v79
	v_mov_b32_e32 v198, v161
	v_mfma_f32_32x32x16_bf16 v[0:15], v[208:211], v[250:253], v[0:15]
	v_max_f32_e32 v205, v160, v160
	v_permlane32_swap_b32_e32 v161, v198
	v_max_f32_e32 v198, v198, v198
	v_max_f32_e32 v161, v161, v161
	v_max_f32_e32 v161, v161, v198
	s_waitcnt lgkmcnt(0)
	v_mfma_f32_32x32x16_bf16 v[32:47], v[128:131], v[238:241], v[32:47]
	ds_read_b64_tr_b16 v[238:239], v174 offset:0x400
	ds_read_b64_tr_b16 v[240:241], v174 offset:0xc00
	v_sub_f32_e32 v198, v161, v160
	v_max_f32_e32 v161, v205, v161
	v_sub_f32_e32 v205, v160, v161
	v_mul_f32_e32 v205, 0x3dd53b94, v205
	v_exp_f32_e32 v205, v205
	v_mfma_f32_32x32x16_bf16 v[32:47], v[132:135], v[242:245], v[32:47]
	ds_read_b64_tr_b16 v[242:243], v174 offset:0x1400
	ds_read_b64_tr_b16 v[244:245], v174 offset:0x1c00
	v_cmp_ge_f32_e32 vcc, s46, v198
	s_cmp_eq_u64 vcc, exec
	s_cselect_b64 s[6:7], -1, 0
	v_cndmask_b32_e64 v205, v205, 1.0, s[6:7]
	v_cndmask_b32_e64 v198, v161, v160, s[6:7]
	v_mul_f32_e32 v236, 0xbdd53b94, v198
	v_mov_b32_e32 v237, v236
	v_cmp_gt_f32_e32 vcc, 1.0, v205
	v_mfma_f32_32x32x16_bf16 v[32:47], v[136:139], v[246:249], v[32:47]
	ds_read_b64_tr_b16 v[246:247], v174 offset:0x2400
	ds_read_b64_tr_b16 v[248:249], v174 offset:0x2c00
	ds_read_b64_tr_b16 v[250:251], v174 offset:0x3400
	ds_read_b64_tr_b16 v[252:253], v174 offset:0x3c00
	v_fmamk_f32 v80, v80, 0x3dd53b94, v236
	v_fmamk_f32 v81, v81, 0x3dd53b94, v236
	v_fmamk_f32 v82, v82, 0x3dd53b94, v236
	v_fmamk_f32 v83, v83, 0x3dd53b94, v236
	v_mfma_f32_32x32x16_bf16 v[32:47], v[208:211], v[162:165], v[32:47]
	v_fmamk_f32 v84, v84, 0x3dd53b94, v236
	v_fmamk_f32 v85, v85, 0x3dd53b94, v236
	v_fmamk_f32 v86, v86, 0x3dd53b94, v236
	v_fmamk_f32 v87, v87, 0x3dd53b94, v236
	s_waitcnt lgkmcnt(0)
	v_mfma_f32_32x32x16_bf16 v[16:31], v[128:131], v[238:241], v[16:31]
	ds_read_b64_tr_b16 v[162:163], v174 offset:0x600
	ds_read_b64_tr_b16 v[164:165], v174 offset:0xe00
	ds_read_b64_tr_b16 v[238:239], v174 offset:0x1600
	ds_read_b64_tr_b16 v[240:241], v174 offset:0x1e00
	v_fmamk_f32 v88, v88, 0x3dd53b94, v236
	v_fmamk_f32 v89, v89, 0x3dd53b94, v236
	v_fmamk_f32 v90, v90, 0x3dd53b94, v236
	v_fmamk_f32 v91, v91, 0x3dd53b94, v236
	v_mfma_f32_32x32x16_bf16 v[16:31], v[132:135], v[242:245], v[16:31]
	ds_read_b64_tr_b16 v[242:243], v174 offset:0x2600
	ds_read_b64_tr_b16 v[244:245], v174 offset:0x2e00
	v_fmamk_f32 v92, v92, 0x3dd53b94, v236
	v_fmamk_f32 v93, v93, 0x3dd53b94, v236
	v_fmamk_f32 v94, v94, 0x3dd53b94, v236
	v_fmamk_f32 v95, v95, 0x3dd53b94, v236
	v_mfma_f32_32x32x16_bf16 v[16:31], v[136:139], v[246:249], v[16:31]
	ds_read_b64_tr_b16 v[246:247], v174 offset:0x3600
	ds_read_b64_tr_b16 v[248:249], v174 offset:0x3e00
	v_exp_f32_e32 v222, v80
	v_exp_f32_e32 v224, v81
	v_exp_f32_e32 v220, v82
	v_mfma_f32_32x32x16_bf16 v[16:31], v[208:211], v[250:253], v[16:31]
	v_exp_f32_e32 v223, v83
	v_exp_f32_e32 v219, v84
	v_exp_f32_e32 v221, v85
	s_waitcnt lgkmcnt(0)
	v_mfma_f32_32x32x16_bf16 v[48:63], v[128:131], v[162:165], v[48:63]
	v_exp_f32_e32 v217, v86
	v_exp_f32_e32 v218, v87
	v_exp_f32_e32 v212, v88
	v_pk_fma_f32 v[130:131], v[70:71], s[26:27], v[236:237] op_sel_hi:[1,0,0]
	v_pk_fma_f32 v[128:129], v[72:73], s[26:27], v[236:237] op_sel_hi:[1,0,0]
	v_mfma_f32_32x32x16_bf16 v[48:63], v[132:135], v[238:241], v[48:63]
	v_exp_f32_e32 v214, v89
	v_exp_f32_e32 v213, v91
	v_exp_f32_e32 v207, v94
	v_pk_fma_f32 v[132:133], v[68:69], s[26:27], v[236:237] op_sel_hi:[1,0,0]
	v_pk_fma_f32 v[134:135], v[78:79], s[26:27], v[236:237] op_sel_hi:[1,0,0]
	v_mfma_f32_32x32x16_bf16 v[48:63], v[136:139], v[242:245], v[48:63]
	v_pk_fma_f32 v[138:139], v[64:65], s[26:27], v[236:237] op_sel_hi:[1,0,0]
	v_pk_fma_f32 v[136:137], v[66:67], s[26:27], v[236:237] op_sel_hi:[1,0,0]
	v_pk_fma_f32 v[162:163], v[74:75], s[26:27], v[236:237] op_sel_hi:[1,0,0]
	v_pk_fma_f32 v[160:161], v[76:77], s[26:27], v[236:237] op_sel_hi:[1,0,0]
	v_mfma_f32_32x32x16_bf16 v[48:63], v[208:211], v[246:249], v[48:63]
	v_exp_f32_e32 v211, v90
	v_exp_f32_e32 v208, v92
	v_exp_f32_e32 v210, v93
	v_exp_f32_e32 v209, v95
	v_add_f32_e32 v64, v203, v204
	v_fmac_f32_e32 v64, v197, v140
	v_add_f32_e32 v140, v215, v216
	s_addk_i32 s13, 0x80
	s_addk_i32 s14, 0x80
	v_fmac_f32_e32 v140, v64, v206
	s_cbranch_vccz .LBB0_2020
	s_and_saveexec_b64 s[10:11], s[4:5]
	ds_write_b32 v189, v205 offset:128
	s_or_b64 exec, exec, s[10:11]
	s_waitcnt lgkmcnt(0)
	v_add_u32_e32 v164, s12, v169
	ds_read_b128 v[238:241], v164 offset:224
	ds_read_b128 v[242:245], v164 offset:192
	ds_read_b128 v[246:249], v164 offset:160
	ds_read_b128 v[250:253], v164 offset:128
	s_waitcnt lgkmcnt(3)
	v_pk_mul_f32 v[12:13], v[12:13], v[238:239]
	s_waitcnt lgkmcnt(2)
	v_pk_mul_f32 v[8:9], v[8:9], v[242:243]
	s_waitcnt lgkmcnt(1)
	v_pk_mul_f32 v[4:5], v[4:5], v[246:247]
	v_pk_mul_f32 v[14:15], v[14:15], v[240:241]
	v_pk_mul_f32 v[10:11], v[10:11], v[244:245]
	v_pk_mul_f32 v[6:7], v[6:7], v[248:249]
	s_waitcnt lgkmcnt(0)
	v_pk_mul_f32 v[2:3], v[2:3], v[252:253]
	v_pk_mul_f32 v[0:1], v[0:1], v[250:251]
	v_pk_mul_f32 v[44:45], v[44:45], v[238:239]
	v_pk_mul_f32 v[40:41], v[40:41], v[242:243]
	v_pk_mul_f32 v[36:37], v[36:37], v[246:247]
	v_pk_mul_f32 v[46:47], v[46:47], v[240:241]
	v_pk_mul_f32 v[42:43], v[42:43], v[244:245]
	v_pk_mul_f32 v[38:39], v[38:39], v[248:249]
	v_pk_mul_f32 v[34:35], v[34:35], v[252:253]
	v_pk_mul_f32 v[32:33], v[32:33], v[250:251]
	v_pk_mul_f32 v[28:29], v[28:29], v[238:239]
	v_pk_mul_f32 v[24:25], v[24:25], v[242:243]
	v_pk_mul_f32 v[20:21], v[20:21], v[246:247]
	v_pk_mul_f32 v[30:31], v[30:31], v[240:241]
	v_pk_mul_f32 v[26:27], v[26:27], v[244:245]
	v_pk_mul_f32 v[22:23], v[22:23], v[248:249]
	v_pk_mul_f32 v[18:19], v[18:19], v[252:253]
	v_pk_mul_f32 v[16:17], v[16:17], v[250:251]
	v_pk_mul_f32 v[60:61], v[60:61], v[238:239]
	v_pk_mul_f32 v[56:57], v[56:57], v[242:243]
	v_pk_mul_f32 v[52:53], v[52:53], v[246:247]
	v_pk_mul_f32 v[62:63], v[62:63], v[240:241]
	v_pk_mul_f32 v[58:59], v[58:59], v[244:245]
	v_pk_mul_f32 v[54:55], v[54:55], v[248:249]
	v_pk_mul_f32 v[50:51], v[50:51], v[252:253]
	v_pk_mul_f32 v[48:49], v[48:49], v[250:251]
